# baseline (speedup 1.0000x reference)
.LBB1_93:
	s_waitcnt vmcnt(0)
	v_mfma_scale_f32_32x32x64_f8f6f4 v[2:17], v[58:65], v[98:105], v[2:17], v201, v201 op_sel_hi:[0,0,0]
	v_lshlrev_b32_e32 v18, 7, v196
	s_waitcnt lgkmcnt(0)
	s_barrier
	ds_read_b128 v[162:165], v18 offset:37376
	ds_read_b128 v[166:169], v18 offset:37392
	ds_read_b128 v[170:173], v18 offset:37408
	ds_read_b128 v[174:177], v18 offset:37424
	ds_read_b128 v[178:181], v18 offset:37440
	ds_read_b128 v[182:185], v18 offset:37456
	ds_read_b128 v[186:189], v18 offset:37472
	ds_read_b128 v[190:193], v18 offset:37488
	s_lshl_b32 s34, s35, 3
	v_or_b32_e32 v202, 0x9100, v18
	s_add_i32 s38, s34, 16
	v_mov_b32_e32 v201, 0
	s_mov_b32 s39, -2
	v_mov_b32_e32 v203, 0x7f7f7f7f
	v_mov_b32_e32 v0, 0
	v_mov_b32_e32 v1, 0
	s_mov_b32 s39, 0
	s_cmp_lt_u32 s52, 4
	s_cbranch_scc1 .Lq2_nostagger
	s_sleep 7
.Lq2_nostagger:
.Lq2_loop:
	s_lshl_b32 s34, s39, 2
	s_add_i32 s34, s34, s35
	s_and_b32 s41, s34, 15
	s_add_i32 s54, s34, 1
	s_and_b32 s54, s54, 15
	s_lshl_b32 s55, s41, 8
	s_lshl_b32 s38, s52, 12
	s_add_i32 s55, s55, s38
	v_lshl_add_u32 v236, v194, 2, s55
	ds_read_b32 v200, v236
	s_lshl_b32 s34, s54, 3
	s_add_i32 s34, s34, s52
	s_lshl_b32 s34, s34, 13
	s_add_i32 s34, s34, s53
	buffer_load_dwordx4 v[146:149], v195, s[44:47], s34 offen
	s_or_b32 s42, s34, 0x400
	buffer_load_dwordx4 v[150:153], v195, s[44:47], s42 offen
	s_or_b32 s43, s34, 0x800
	buffer_load_dwordx4 v[154:157], v195, s[44:47], s43 offen
	s_or_b32 s42, s34, 0xc00
	buffer_load_dwordx4 v[158:161], v195, s[44:47], s42 offen
	s_or_b32 s43, s34, 0x1000
	buffer_load_dwordx4 v[138:141], v195, s[44:47], s43 offen
	s_or_b32 s42, s34, 0x1400
	buffer_load_dwordx4 v[142:145], v195, s[44:47], s42 offen
	s_or_b32 s43, s34, 0x1800
	buffer_load_dwordx4 v[130:133], v195, s[44:47], s43 offen
	s_or_b32 s42, s34, 0x1c00
	buffer_load_dwordx4 v[134:137], v195, s[44:47], s42 offen
	s_lshl_b32 s55, s41, 3
	s_add_i32 s55, s55, s52
	s_cmp_lg_u32 s55, s33
	s_cbranch_scc1 .Lq2_nd0_0
	v_cndmask_b32_e64 v2, v2, v198, s[0:1]
	v_cndmask_b32_e64 v3, v3, v198, s[2:3]
	v_cndmask_b32_e64 v4, v4, v198, s[4:5]
	v_cndmask_b32_e64 v5, v5, v198, s[6:7]
	v_cndmask_b32_e64 v6, v6, v198, s[8:9]
	v_cndmask_b32_e64 v7, v7, v198, s[10:11]
	v_cndmask_b32_e64 v8, v8, v198, s[12:13]
	v_cndmask_b32_e64 v9, v9, v198, s[14:15]
	v_cndmask_b32_e64 v10, v10, v198, s[16:17]
	v_cndmask_b32_e64 v11, v11, v198, s[18:19]
	v_cndmask_b32_e64 v12, v12, v198, s[20:21]
	v_cndmask_b32_e64 v13, v13, v198, s[22:23]
	v_cndmask_b32_e64 v14, v14, v198, s[24:25]
	v_cndmask_b32_e64 v15, v15, v198, s[26:27]
	v_cndmask_b32_e64 v16, v16, v198, s[28:29]
	v_cndmask_b32_e64 v17, v17, v198, s[30:31]
